# P1: waves 4-7 run the rmsnorm rows before the weight conversion (waves 0-3 the reverse), plus nt hint on once-read f32 weight loads and final output stores
# baseline (speedup 1.0000x reference)
.LBB0_15:
	s_or_b64 exec, exec, s[6:7]
	v_readlane_b32 s23, v252, 0
	s_ashr_i32 s6, s23, 31
	v_writelane_b32 v252, s6, 5
	s_lshr_b32 s6, s6, 29
	s_add_i32 s6, s23, s6
	s_ashr_i32 s24, s6, 3
	s_lshr_b32 s10, s8, 6
	s_mul_i32 s7, s24, 0xffffff01
	v_writelane_b32 v252, s10, 6
	s_lshl_b32 s10, s23, 5
	s_add_i32 s12, s7, s10
	s_lshl_b32 s7, s12, 3
	s_add_u32 s0, s0, 0x110
	v_writelane_b32 v252, s7, 7
	s_addc_u32 s1, s1, 0
	v_writelane_b32 v252, s0, 8
	s_mov_b32 s38, 0x6dc9c883
	v_mov_b32_e32 v161, 0
	v_writelane_b32 v252, s1, 9
	v_mov_b32_e32 v240, 0x358637bd
	v_readlane_b32 s10, v252, 1
	v_readlane_b32 s11, v252, 2
	s_add_u32 s0, s10, 0x4200
	s_addc_u32 s1, s11, 0
	v_writelane_b32 v252, s0, 10
	s_mov_b32 s39, 0x3fc45f30
	v_mov_b32_e32 v225, 0x3c0881c4
	v_writelane_b32 v252, s1, 11
	s_add_u32 s0, s10, 0x4400
	s_addc_u32 s1, s11, 0
	v_writelane_b32 v252, s0, 12
	v_mov_b32_e32 v226, 0xbab64f3b
	v_mov_b32_e32 v245, 0x3b808081
	v_writelane_b32 v252, s1, 13
	s_add_u32 s0, s10, 0x4500
	s_addc_u32 s1, s11, 0
	v_writelane_b32 v252, s0, 14
	v_mov_b32_e32 v242, 0x7f800000
	v_not_b32_e32 v227, 63
	v_writelane_b32 v252, s1, 15
	s_add_u32 s0, s10, 0x4600
	s_addc_u32 s1, s11, 0
	v_writelane_b32 v252, s0, 16
	v_not_b32_e32 v250, 31
	v_mov_b32_e32 v251, 0x7fc00000
	v_writelane_b32 v252, s1, 17
	s_add_u32 s0, s10, 0x4700
	s_addc_u32 s1, s11, 0
	v_writelane_b32 v252, s0, 18
	v_mov_b32_e32 v243, 0xc2700000
	s_movk_i32 s76, 0x1a00
	v_writelane_b32 v252, s1, 19
	s_add_u32 s0, s10, 0x4800
	s_addc_u32 s1, s11, 0
	v_writelane_b32 v252, s0, 20
	s_mov_b32 s67, 0x6468000
	s_mov_b32 s72, 0
	v_writelane_b32 v252, s1, 21
	s_add_u32 s0, s10, 0x4900
	s_addc_u32 s1, s11, 0
	v_writelane_b32 v252, s0, 22
	s_mov_b32 s97, 0
	v_writelane_b32 v255, s97, 62
	s_mov_b64 s[84:85], -1
	v_writelane_b32 v252, s1, 23
	s_add_u32 s0, s10, 0x4a00
	s_addc_u32 s1, s11, 0
	v_writelane_b32 v252, s0, 24
	s_mov_b64 s[60:61], 0x40000
	s_mov_b64 s[52:53], 0x60000
	v_writelane_b32 v252, s1, 25
	s_add_u32 s0, s10, 0x4b00
	s_addc_u32 s1, s11, 0
	v_writelane_b32 v252, s0, 26
	s_mov_b64 s[56:57], 0x80
	s_mov_b64 s[26:27], 0x60080
	v_writelane_b32 v252, s1, 27
	s_add_u32 s0, s10, 0x4c00
	s_addc_u32 s1, s11, 0
	v_writelane_b32 v252, s0, 28
	s_mov_b32 s30, 0x3b800000
	s_mov_b64 s[28:29], 0x10080
	v_writelane_b32 v252, s1, 29
	s_add_u32 s0, s10, 0x4d00
	s_addc_u32 s1, s11, 0
	v_writelane_b32 v252, s0, 30
	s_mov_b32 s62, 0x3e38aa3b
	s_mov_b32 s66, 0x3e16c740
	v_writelane_b32 v252, s1, 31
	s_add_u32 s0, s10, 0x4e00
	s_addc_u32 s1, s11, 0
	v_writelane_b32 v252, s0, 32
	s_mov_b64 s[68:69], 0x2a400
	s_mov_b64 s[70:71], 0x2be00
	v_writelane_b32 v252, s1, 33
	s_add_u32 s0, s10, 0x4f00
	s_addc_u32 s1, s11, 0
	v_writelane_b32 v252, s0, 34
	s_mov_b32 s82, 0x3b808081
	s_mov_b32 s94, 0x37800000
	v_writelane_b32 v252, s1, 35
	s_add_u32 s0, s10, 0x5000
	s_addc_u32 s1, s11, 0
	v_writelane_b32 v252, s0, 36
	s_waitcnt lgkmcnt(0)
	s_barrier
	v_writelane_b32 v252, s1, 37
	s_add_u32 s0, s10, 0x5100
	s_addc_u32 s1, s11, 0
	v_writelane_b32 v252, s0, 38
	s_nop 1
	v_writelane_b32 v252, s1, 39
	s_add_u32 s0, s10, 0x5200
	s_addc_u32 s1, s11, 0
	v_writelane_b32 v252, s0, 40
	s_nop 1
	v_writelane_b32 v252, s1, 41
	s_add_u32 s0, s10, 0x5300
	s_addc_u32 s1, s11, 0
	v_writelane_b32 v252, s0, 42
	s_cmp_eq_u32 s9, 15
	s_nop 0
	v_writelane_b32 v252, s1, 43
	s_cselect_b64 s[0:1], -1, 0
	v_writelane_b32 v252, s0, 44
	s_cmp_eq_u32 s9, 14
	s_nop 0
	v_writelane_b32 v252, s1, 45
	s_cselect_b64 s[0:1], -1, 0
	v_writelane_b32 v252, s0, 46
	s_cmp_eq_u32 s9, 13
	s_nop 0
	v_writelane_b32 v252, s1, 47
	s_cselect_b64 s[0:1], -1, 0
	v_writelane_b32 v252, s0, 48
	s_cmp_eq_u32 s9, 12
	s_nop 0
	v_writelane_b32 v252, s1, 49
	s_cselect_b64 s[0:1], -1, 0
	v_writelane_b32 v252, s0, 50
	s_cmp_eq_u32 s9, 11
	s_nop 0
	v_writelane_b32 v252, s1, 51
	s_cselect_b64 s[0:1], -1, 0
	v_writelane_b32 v252, s0, 52
	s_cmp_eq_u32 s9, 10
	s_nop 0
	v_writelane_b32 v252, s1, 53
	s_cselect_b64 s[0:1], -1, 0
	v_writelane_b32 v252, s0, 54
	s_cmp_eq_u32 s9, 9
	s_nop 0
	v_writelane_b32 v252, s1, 55
	s_cselect_b64 s[0:1], -1, 0
	v_writelane_b32 v252, s0, 56
	s_cmp_eq_u32 s9, 8
	s_nop 0
	v_writelane_b32 v252, s1, 57
	s_cselect_b64 s[0:1], -1, 0
	v_writelane_b32 v252, s0, 58
	s_cmp_eq_u32 s9, 7
	s_nop 0
	v_writelane_b32 v252, s1, 59
	s_cselect_b64 s[0:1], -1, 0
	v_writelane_b32 v252, s0, 60
	s_cmp_eq_u32 s9, 6
	s_nop 0
	v_writelane_b32 v252, s1, 61
	s_cselect_b64 s[0:1], -1, 0
	v_writelane_b32 v252, s0, 62
	s_cmp_eq_u32 s9, 5
	s_nop 0
	v_writelane_b32 v252, s1, 63
	s_cselect_b64 s[0:1], -1, 0
	v_writelane_b32 v253, s0, 0
	s_cmp_eq_u32 s9, 4
	s_nop 0
	v_writelane_b32 v253, s1, 1
	s_cselect_b64 s[0:1], -1, 0
	v_writelane_b32 v253, s0, 2
	s_cmp_eq_u32 s9, 3
	s_nop 0
	v_writelane_b32 v253, s1, 3
	s_cselect_b64 s[0:1], -1, 0
	v_writelane_b32 v253, s0, 4
	s_cmp_eq_u32 s9, 2
	s_nop 0
	v_writelane_b32 v253, s1, 5
	s_cselect_b64 s[0:1], -1, 0
	v_writelane_b32 v253, s0, 6
	s_cmp_eq_u32 s9, 1
	s_nop 0
	v_writelane_b32 v253, s1, 7
	s_cselect_b64 s[0:1], -1, 0
	v_writelane_b32 v253, s0, 8
	s_cmp_eq_u32 s9, 0
	s_nop 0
	v_writelane_b32 v253, s1, 9
	s_cselect_b64 s[0:1], -1, 0
	v_writelane_b32 v253, s0, 10
	s_nop 1
	v_writelane_b32 v253, s1, 11
	s_lshl_b32 s0, s9, 8
	s_add_u32 s0, s4, s0
	s_addc_u32 s1, s5, 0
	s_add_u32 s4, s0, 0x1400
	s_addc_u32 s5, s1, 0
	v_writelane_b32 v253, s4, 12
	s_add_u32 s0, s0, 0x2400
	s_addc_u32 s1, s1, 0
	v_writelane_b32 v253, s5, 13
	v_writelane_b32 v253, s0, 14
	s_nop 1
	v_writelane_b32 v253, s1, 15
	s_add_u32 s0, s10, 0x7400
	s_addc_u32 s1, s11, 0
	v_writelane_b32 v253, s0, 16
	s_nop 1
	v_writelane_b32 v253, s1, 17
	s_add_u32 s0, s10, 0x7500
	s_addc_u32 s1, s11, 0
	v_writelane_b32 v253, s0, 18
	s_nop 1
	v_writelane_b32 v253, s1, 19
	s_and_b32 s0, s8, 0xffffffc0
	s_cmpk_lt_i32 s23, 0x680
	v_writelane_b32 v253, s0, 20
	s_cselect_b64 s[0:1], -1, 0
	v_writelane_b32 v253, s0, 21
	s_nop 1
	v_writelane_b32 v253, s1, 22
	s_add_i32 s0, s23, 0x80
	s_ashr_i32 s1, s0, 31
	s_lshr_b32 s1, s1, 24
	s_add_i32 s1, s0, s1
	s_and_b32 s1, s1, 0xffffff00
	s_sub_i32 s7, s0, s1
	s_and_b32 s0, s6, -8
	s_sub_i32 s16, s23, s0
	s_cmp_lt_i32 s7, 64
	s_sext_i32_i16 s1, s7
	s_cselect_b64 s[4:5], -1, 0
	s_bfe_u32 s1, s1, 0x3001c
	v_writelane_b32 v253, s4, 23
	s_add_i32 s1, s7, s1
	s_ashr_i32 s6, s7, 31
	v_writelane_b32 v253, s5, 24
	s_sext_i32_i16 s4, s1
	s_and_b32 s1, s1, 0xfff8
	s_sub_i32 s1, s7, s1
	s_ashr_i32 s4, s4, 3
	s_lshl_b32 s5, s1, 3
	v_writelane_b32 v253, s7, 25
	s_cmpk_lt_i32 s23, 0x380
	v_writelane_b32 v253, s6, 26
	s_cselect_b64 s[6:7], -1, 0
	v_writelane_b32 v253, s6, 27
	s_cmpk_lt_i32 s12, 0x200
	s_nop 0
	v_writelane_b32 v253, s7, 28
	s_cselect_b64 s[6:7], -1, 0
	v_writelane_b32 v253, s6, 29
	s_cmpk_gt_u32 s8, 0xff
	s_nop 0
	v_writelane_b32 v253, s7, 30
	s_cselect_b64 s[6:7], -1, 0
	v_writelane_b32 v253, s6, 31
	s_cmpk_lt_i32 s23, 0x800
	s_nop 0
	v_writelane_b32 v253, s7, 32
	s_cselect_b64 s[6:7], -1, 0
	v_writelane_b32 v253, s6, 33
	s_nop 1
	v_writelane_b32 v253, s7, 34
	s_lshl_b32 s6, s16, 8
	s_cmpk_lt_i32 s23, 0x200
	s_cselect_b64 s[8:9], -1, 0
	s_lshl_b32 s7, s16, 6
	v_writelane_b32 v253, s8, 35
	s_cmpk_lt_i32 s23, 0xe00
	s_cselect_b64 s[10:11], -1, 0
	v_writelane_b32 v253, s9, 36
	s_mul_hi_i32 s8, s23, 0x92492493
	v_writelane_b32 v253, s10, 37
	s_add_i32 s8, s8, s23
	s_lshr_b32 s9, s8, 31
	v_writelane_b32 v253, s11, 38
	v_writelane_b32 v253, s8, 39
	s_ashr_i32 s8, s8, 2
	v_writelane_b32 v253, s9, 40
	s_add_i32 s8, s8, s9
	v_writelane_b32 v253, s8, 41
	s_add_i32 s0, s0, 0xffb0
	s_mul_i32 s8, s8, 7
	v_writelane_b32 v253, s0, 42
	s_sub_i32 s8, s23, s8
	v_writelane_b32 v253, s12, 43
	s_lshl_b32 s0, s12, 7
	s_ashr_i32 s9, s8, 31
	v_writelane_b32 v253, s0, 44
	s_mov_b32 s0, s8
	v_writelane_b32 v253, s0, 45
	s_lshl_b64 s[8:9], s[8:9], 9
	s_cmp_lt_i32 s16, 0
	v_writelane_b32 v253, s1, 46
	s_mul_i32 s0, s16, 0x101
	s_cselect_b32 s0, s0, s6
	s_mul_i32 s6, s16, 0x41
	s_cselect_b32 s6, s6, s7
	s_movk_i32 s7, 0xd1
	v_writelane_b32 v253, s8, 47
	s_cselect_b32 s7, s7, 0xd0
	s_mul_i32 s7, s16, s7
	v_writelane_b32 v253, s9, 48
	s_movk_i32 s8, 0x71
	s_movk_i32 s9, 0x1c1
	s_cselect_b32 s8, s8, 0x70
	s_cselect_b32 s9, s9, 0x1c0
	s_add_i32 s7, s7, s24
	s_mul_hi_i32 s10, s7, 0x4ec4ec4f
	s_lshr_b32 s11, s10, 31
	s_ashr_i32 s10, s10, 5
	s_add_i32 s10, s10, s11
	s_mul_i32 s11, s10, 0x68
	s_lshl_b32 s10, s10, 3
	s_sub_i32 s7, s7, s11
	s_sub_i32 s11, 0x80, s10
	s_min_i32 s11, s11, 8
	s_sext_i32_i16 s12, s1
	s_cmp_lt_i32 s12, 0
	s_mul_i32 s1, s1, 9
	s_cselect_b32 s1, s1, s5
	s_add_i32 s1, s1, s4
	s_bfe_i32 s4, s1, 0x80000
	s_bfe_u32 s4, s4, 0x5000a
	s_add_i32 s4, s1, s4
	s_and_b32 s5, s4, 0xffe0
	s_sub_i32 s1, s1, s5
	s_bfe_i32 s5, s1, 0x80000
	s_bfe_u32 s5, s5, 0x3000c
	s_add_i32 s5, s1, s5
	s_mul_i32 s8, s16, s8
	s_and_b32 s12, s5, 0xf8
	s_add_i32 s8, s8, s24
	s_sub_i32 s1, s1, s12
	s_mul_hi_i32 s12, s8, 0x92492493
	s_add_i32 s12, s12, s8
	s_lshr_b32 s13, s12, 31
	s_ashr_i32 s12, s12, 5
	s_add_i32 s12, s12, s13
	s_mul_i32 s13, s12, 56
	s_add_i32 s0, s0, s24
	s_sub_i32 s8, s8, s13
	s_ashr_i32 s13, s0, 31
	s_lshr_b32 s13, s13, 25
	s_add_i32 s13, s0, s13
	s_and_b32 s14, s13, 0xffffff80
	s_add_i32 s6, s6, s24
	s_sub_i32 s0, s0, s14
	s_ashr_i32 s14, s6, 31
	s_lshr_b32 s14, s14, 27
	s_add_i32 s14, s6, s14
	s_mul_i32 s9, s16, s9
	s_and_b32 s15, s14, 0xffffffe0
	s_add_i32 s9, s9, s24
	s_sub_i32 s6, s6, s15
	s_mul_hi_i32 s15, s9, 0x92492493
	s_add_i32 s15, s15, s9
	v_writelane_b32 v253, s16, 49
	s_lshr_b32 s16, s15, 31
	s_ashr_i32 s15, s15, 7
	s_add_i32 s15, s15, s16
	s_mul_i32 s16, s15, 0xe0
	s_sub_i32 s9, s9, s16
	s_abs_i32 s16, s11
	v_cvt_f32_u32_e32 v0, s16
	s_bfe_i32 s4, s4, 0x80000
	s_sub_i32 s17, 0, s16
	s_sext_i32_i16 s4, s4
	v_rcp_iflag_f32_e32 v0, v0
	s_ashr_i32 s4, s4, 5
	s_lshl_b32 s4, s4, 3
	s_bfe_i32 s5, s5, 0x80000
	v_mul_f32_e32 v0, 0x4f7ffffe, v0
	v_cvt_u32_f32_e32 v0, v0
	s_sext_i32_i8 s1, s1
	s_sext_i32_i16 s5, s5
	s_add_i32 s4, s4, s1
	v_readfirstlane_b32 s18, v0
	s_mul_i32 s17, s17, s18
	s_mul_hi_u32 s17, s18, s17
	s_add_i32 s18, s18, s17
	s_abs_i32 s17, s7
	s_mul_hi_u32 s18, s17, s18
	v_writelane_b32 v253, s4, 50
	s_lshl_b32 s1, s12, 3
	s_ashr_i32 s12, s13, 7
	s_ashr_i32 s14, s14, 5
	s_mul_i32 s19, s18, s16
	v_writelane_b32 v253, s5, 51
	s_lshl_b32 s12, s12, 3
	s_lshl_b32 s14, s14, 3
	s_lshl_b32 s15, s15, 3
	s_ashr_i32 s22, s5, 3
	s_sub_i32 s17, s17, s19
	s_sub_i32 s4, 0x80, s1
	s_sub_i32 s13, 0x80, s12
	s_sub_i32 s19, 0x80, s14
	s_sub_i32 s20, 0x80, s15
	s_xor_b32 s21, s7, s11
	v_writelane_b32 v253, s22, 52
	s_min_i32 s4, s4, 8
	s_min_i32 s13, s13, 8
	s_min_i32 s19, s19, 8
	s_min_i32 s20, s20, 8
	s_ashr_i32 s21, s21, 31
	v_writelane_b32 v253, s23, 53
	s_add_i32 s5, s18, 1
	s_sub_i32 s22, s17, s16
	s_cmp_ge_u32 s17, s16
	s_cselect_b32 s5, s5, s18
	s_cselect_b32 s17, s22, s17
	s_add_i32 s18, s5, 1
	s_cmp_ge_u32 s17, s16
	s_cselect_b32 s5, s18, s5
	s_xor_b32 s5, s5, s21
	s_sub_i32 s18, s5, s21
	s_mul_i32 s5, s18, s11
	s_sub_i32 s5, s7, s5
	s_abs_i32 s7, s4
	v_cvt_f32_u32_e32 v0, s7
	s_mov_b32 s16, s18
	v_writelane_b32 v253, s16, 54
	s_sub_i32 s11, 0, s7
	v_rcp_iflag_f32_e32 v0, v0
	v_writelane_b32 v253, s17, 55
	s_add_i32 s10, s10, s5
	s_xor_b32 s5, s8, s4
	v_mul_f32_e32 v0, 0x4f7ffffe, v0
	v_cvt_u32_f32_e32 v0, v0
	s_ashr_i32 s5, s5, 31
	v_readfirstlane_b32 s16, v0
	s_mul_i32 s11, s11, s16
	s_mul_hi_u32 s11, s16, s11
	s_add_i32 s16, s16, s11
	s_abs_i32 s11, s8
	s_mul_hi_u32 s16, s11, s16
	s_mul_i32 s17, s16, s7
	s_sub_i32 s11, s11, s17
	v_writelane_b32 v253, s10, 56
	s_sub_i32 s17, s11, s7
	s_nop 0
	v_writelane_b32 v253, s11, 57
	s_add_i32 s10, s16, 1
	s_cmp_ge_u32 s11, s7
	s_cselect_b32 s10, s10, s16
	s_cselect_b32 s11, s17, s11
	s_add_i32 s16, s10, 1
	s_cmp_ge_u32 s11, s7
	s_cselect_b32 s7, s16, s10
	s_xor_b32 s7, s7, s5
	s_sub_i32 s5, s7, s5
	v_writelane_b32 v253, s5, 58
	s_mul_i32 s4, s5, s4
	s_abs_i32 s5, s13
	v_cvt_f32_u32_e32 v0, s5
	s_sub_i32 s4, s8, s4
	s_sub_i32 s7, 0, s5
	s_add_i32 s4, s1, s4
	v_rcp_iflag_f32_e32 v0, v0
	s_xor_b32 s1, s0, s13
	s_ashr_i32 s1, s1, 31
	s_mov_b64 s[16:17], 0x30000
	v_mul_f32_e32 v0, 0x4f7ffffe, v0
	v_cvt_u32_f32_e32 v0, v0
	s_nop 0
	v_readfirstlane_b32 s8, v0
	s_mul_i32 s7, s7, s8
	s_mul_hi_u32 s7, s8, s7
	s_add_i32 s8, s8, s7
	s_abs_i32 s7, s0
	s_mul_hi_u32 s8, s7, s8
	s_mul_i32 s10, s8, s5
	s_sub_i32 s7, s7, s10
	v_writelane_b32 v253, s4, 59
	s_sub_i32 s10, s7, s5
	s_nop 0
	v_writelane_b32 v253, s5, 60
	s_add_i32 s4, s8, 1
	s_cmp_ge_u32 s7, s5
	s_cselect_b32 s4, s4, s8
	s_cselect_b32 s7, s10, s7
	s_add_i32 s8, s4, 1
	s_cmp_ge_u32 s7, s5
	s_cselect_b32 s4, s8, s4
	s_xor_b32 s4, s4, s1
	s_sub_i32 s8, s4, s1
	s_mul_i32 s1, s8, s13
	s_sub_i32 s0, s0, s1
	s_abs_i32 s1, s19
	v_cvt_f32_u32_e32 v0, s1
	s_mov_b32 s4, s8
	v_writelane_b32 v253, s4, 61
	s_add_i32 s0, s12, s0
	v_rcp_iflag_f32_e32 v0, v0
	v_writelane_b32 v253, s5, 62
	s_sub_i32 s4, 0, s1
	v_mul_f32_e32 v0, 0x4f7ffffe, v0
	v_cvt_u32_f32_e32 v0, v0
	s_nop 0
	v_readfirstlane_b32 s5, v0
	s_mul_i32 s4, s4, s5
	s_mul_hi_u32 s4, s5, s4
	s_add_i32 s5, s5, s4
	s_abs_i32 s4, s6
	s_mul_hi_u32 s5, s4, s5
	s_mul_i32 s7, s5, s1
	v_writelane_b32 v253, s0, 63
	s_sub_i32 s4, s4, s7
	s_add_i32 s7, s5, 1
	v_writelane_b32 v254, s1, 0
	s_xor_b32 s0, s6, s19
	s_ashr_i32 s0, s0, 31
	s_sub_i32 s8, s4, s1
	s_cmp_ge_u32 s4, s1
	s_cselect_b32 s5, s7, s5
	s_cselect_b32 s4, s8, s4
	s_add_i32 s7, s5, 1
	s_cmp_ge_u32 s4, s1
	s_cselect_b32 s1, s7, s5
	s_xor_b32 s1, s1, s0
	s_sub_i32 s4, s1, s0
	s_mov_b32 s0, s4
	v_writelane_b32 v254, s0, 1
	s_nop 1
	v_writelane_b32 v254, s1, 2
	s_abs_i32 s1, s20
	v_cvt_f32_u32_e32 v0, s1
	s_mul_i32 s0, s4, s19
	s_sub_i32 s4, 0, s1
	s_sub_i32 s0, s6, s0
	v_rcp_iflag_f32_e32 v0, v0
	s_add_i32 s0, s14, s0
	v_mul_f32_e32 v0, 0x4f7ffffe, v0
	v_cvt_u32_f32_e32 v0, v0
	s_nop 0
	v_readfirstlane_b32 s5, v0
	s_mul_i32 s4, s4, s5
	s_mul_hi_u32 s4, s5, s4
	s_add_i32 s5, s5, s4
	s_abs_i32 s4, s9
	s_mul_hi_u32 s5, s4, s5
	s_mul_i32 s6, s5, s1
	v_writelane_b32 v254, s0, 3
	s_sub_i32 s4, s4, s6
	s_add_i32 s6, s5, 1
	v_writelane_b32 v254, s1, 4
	s_xor_b32 s0, s9, s20
	s_ashr_i32 s0, s0, 31
	s_sub_i32 s7, s4, s1
	s_cmp_ge_u32 s4, s1
	s_cselect_b32 s5, s6, s5
	s_cselect_b32 s4, s7, s4
	s_add_i32 s6, s5, 1
	s_cmp_ge_u32 s4, s1
	s_cselect_b32 s1, s6, s5
	s_xor_b32 s1, s1, s0
	s_sub_i32 s4, s1, s0
	s_mov_b32 s0, s4
	v_writelane_b32 v254, s0, 5
	s_mul_i32 s5, s24, 0xff0
	s_nop 0
	v_writelane_b32 v254, s1, 6
	s_mul_i32 s0, s4, s20
	s_lshl_b32 s1, s23, 8
	s_mul_i32 s4, s24, 0x7f8
	s_sub_i32 s1, s1, s4
	s_lshl_b32 s4, s23, 9
	s_sub_i32 s4, s4, s5
	v_writelane_b32 v254, s4, 7
	s_lshl_b32 s4, s23, 12
	s_mul_i32 s5, s24, 0x7f80
	s_sub_i32 s0, s9, s0
	v_writelane_b32 v254, s24, 8
	s_sub_i32 s4, s4, s5
	v_writelane_b32 v254, s4, 9
	s_add_i32 s0, s15, s0
	v_writelane_b32 v254, s0, 10
	s_mov_b64 s[8:9], 0x10000
	s_mov_b64 s[14:15], 0x20000
	v_writelane_b32 v254, s1, 11
	s_add_i32 s0, s1, 0xfffff800
	v_writelane_b32 v254, s0, 12
	s_add_u32 s0, s2, 0x800
	v_writelane_b32 v254, s0, 13
	s_addc_u32 s0, s3, 0
	v_writelane_b32 v254, s0, 14
	s_add_i32 s0, 0, 0x20488
	v_writelane_b32 v254, s0, 15
	s_add_i32 s0, 0, 0x2048c
	v_writelane_b32 v254, s0, 16
	s_add_i32 s0, 0, 0x20460
	v_writelane_b32 v254, s0, 17
	s_add_i32 s0, 0, 0x20464
	v_writelane_b32 v254, s0, 18
	s_add_i32 s0, 0, 0x20458
	v_writelane_b32 v254, s0, 19
	s_add_i32 s0, 0, 0x2045c
	v_writelane_b32 v254, s0, 20
	s_add_i32 s0, 0, 0x204b8
	v_writelane_b32 v254, s0, 21
	s_add_i32 s0, 0, 0x204bc
	v_writelane_b32 v254, s0, 22
	s_add_i32 s0, 0, 0x204a0
	v_writelane_b32 v254, s0, 23
	s_add_i32 s0, 0, 0x204a4
	v_writelane_b32 v254, s0, 24
	s_add_i32 s0, 0, 0x204a8
	v_writelane_b32 v254, s0, 25
	s_add_i32 s0, 0, 0x204ac
	v_writelane_b32 v254, s0, 26
	s_add_i32 s0, 0, 0x20420
	v_writelane_b32 v254, s0, 27
	s_add_i32 s0, 0, 0x20424
	v_writelane_b32 v254, s0, 28
	s_add_i32 s0, 0, 0x20410
	v_writelane_b32 v254, s0, 29
	s_add_i32 s0, 0, 0x20414
	v_writelane_b32 v254, s0, 30
	s_add_i32 s0, 0, 0x20400
	v_writelane_b32 v254, s0, 31
	s_add_i32 s0, 0, 0x20404
	v_writelane_b32 v254, s0, 32
	s_add_i32 s0, 0, 0x20408
	v_writelane_b32 v254, s0, 33
	s_add_i32 s0, 0, 0x2040c
	v_writelane_b32 v254, s0, 34
	s_add_i32 s0, 0, 0x20418
	v_writelane_b32 v254, s0, 35
	s_add_i32 s0, 0, 0x2041c
	v_writelane_b32 v254, s0, 36
	s_add_i32 s0, 0, 0x20160
	v_writelane_b32 v254, s0, 37
	s_add_i32 s0, 0, 0x20164
	v_writelane_b32 v254, s0, 38
	s_add_i32 s0, 0, 0x20430
	v_writelane_b32 v254, s0, 39
	s_add_i32 s0, 0, 0x20434
	v_writelane_b32 v254, s0, 40
	s_add_i32 s0, 0, 0x20480
	v_writelane_b32 v254, s0, 41
	s_add_i32 s0, 0, 0x20484
	v_writelane_b32 v254, s0, 42
	s_add_i32 s0, 0, 0x20498
	v_writelane_b32 v254, s0, 43
	s_add_i32 s0, 0, 0x2049c
	v_writelane_b32 v254, s0, 44
	s_add_i32 s0, 0, 0x20448
	v_writelane_b32 v254, s0, 45
	s_add_i32 s0, 0, 0x2044c
	v_writelane_b32 v254, s0, 46
	s_add_i32 s0, 0, 0x20450
	v_writelane_b32 v254, s0, 47
	s_add_i32 s0, 0, 0x20454
	v_writelane_b32 v254, s0, 48
	s_add_i32 s0, 0, 0x20470
	v_writelane_b32 v254, s0, 49
	s_add_i32 s0, 0, 0x20474
	v_writelane_b32 v254, s0, 50
	s_add_i32 s0, 0, 0x20428
	v_writelane_b32 v254, s0, 51
	s_add_i32 s0, 0, 0x2042c
	v_writelane_b32 v254, s0, 52
	s_add_i32 s0, 0, 0x20468
	v_writelane_b32 v254, s0, 53
	s_add_i32 s0, 0, 0x2046c
	v_writelane_b32 v254, s0, 54
	s_add_i32 s0, 0, 0x20478
	v_writelane_b32 v254, s0, 55
	s_add_i32 s0, 0, 0x2047c
	v_writelane_b32 v254, s0, 56
	s_add_i32 s0, 0, 0x20490
	v_writelane_b32 v254, s0, 57
	s_add_i32 s0, 0, 0x20494
	v_writelane_b32 v254, s0, 58
	s_add_i32 s0, 0, 0x20438
	v_writelane_b32 v254, s0, 59
	s_add_i32 s0, 0, 0x2043c
	v_writelane_b32 v254, s0, 60
	s_add_i32 s0, 0, 0x20440
	v_writelane_b32 v254, s0, 61
	s_add_i32 s0, 0, 0x20444
	v_writelane_b32 v254, s0, 62
	s_add_i32 s0, 0, 0x204b0
	v_writelane_b32 v254, s0, 63
	s_add_i32 s0, 0, 0x204b4
	v_writelane_b32 v255, s0, 0
	s_add_i32 s0, 0, 0x204c8
	v_writelane_b32 v255, s0, 1
	s_add_i32 s0, 0, 0x204cc
	v_writelane_b32 v255, s0, 2
	s_add_i32 s0, 0, 0x204d0
	v_writelane_b32 v255, s0, 3
	s_add_i32 s0, 0, 0x204d4
	v_writelane_b32 v255, s0, 4
	s_add_i32 s0, 0, 0x204d8
	v_writelane_b32 v255, s0, 5
	s_add_i32 s0, 0, 0x204dc
	v_writelane_b32 v255, s0, 6
	s_add_i32 s0, 0, 0x204c0
	v_writelane_b32 v255, s0, 7
	s_add_i32 s0, 0, 0x204c4
	v_writelane_b32 v255, s0, 8
	s_add_i32 s0, 0, 0x204e8
	v_writelane_b32 v255, s0, 9
	s_add_i32 s0, 0, 0x204ec
	v_writelane_b32 v255, s0, 10
	s_add_i32 s0, 0, 0x204f0
	v_writelane_b32 v255, s0, 11
	s_add_i32 s0, 0, 0x204f4
	v_writelane_b32 v255, s0, 12
	s_add_i32 s0, 0, 0x204f8
	v_writelane_b32 v255, s0, 13
	s_add_i32 s0, 0, 0x204fc
	v_writelane_b32 v255, s0, 14
	s_add_i32 s0, 0, 0x204e0
	v_writelane_b32 v255, s0, 15
	s_add_i32 s0, 0, 0x204e4
	v_writelane_b32 v255, s0, 16
	s_add_i32 s0, 0, 0x21060
	v_writelane_b32 v255, s0, 17
	s_add_i32 s0, 0, 0x21020
	v_writelane_b32 v255, s0, 18
	s_add_i32 s0, 0, 0x21064
	v_writelane_b32 v255, s0, 19
	s_add_i32 s0, 0, 0x21024
	v_writelane_b32 v255, s0, 20
	s_add_i32 s0, 0, 0x21068
	v_writelane_b32 v255, s0, 21
	s_add_i32 s0, 0, 0x21028
	v_writelane_b32 v255, s0, 22
	s_add_i32 s0, 0, 0x2106c
	v_writelane_b32 v255, s0, 23
	s_add_i32 s0, 0, 0x2102c
	v_writelane_b32 v255, s0, 24
	s_add_i32 s0, 0, 0x21070
	v_writelane_b32 v255, s0, 25
	s_add_i32 s0, 0, 0x21030
	v_writelane_b32 v255, s0, 26
	s_add_i32 s0, 0, 0x21074
	v_writelane_b32 v255, s0, 27
	s_add_i32 s0, 0, 0x21034
	v_writelane_b32 v255, s0, 28
	s_add_i32 s0, 0, 0x21078
	v_writelane_b32 v255, s0, 29
	s_add_i32 s0, 0, 0x21038
	v_writelane_b32 v255, s0, 30
	s_add_i32 s0, 0, 0x2107c
	v_writelane_b32 v255, s0, 31
	s_add_i32 s0, 0, 0x2103c
	v_writelane_b32 v255, s0, 32
	s_add_i32 s0, 0, 0x21080
	v_writelane_b32 v255, s0, 33
	s_mov_b64 s[0:1], 0
	v_writelane_b32 v255, s0, 34
	s_mov_b64 s[20:21], 0x38000
	s_mov_b64 s[24:25], 0x40080
	v_writelane_b32 v255, s1, 35
	s_mov_b64 s[0:1], 0x20080
	s_branch .LBB0_17

.LBB0_17:
	v_readlane_b32 s36, v252, 1
	v_readlane_b32 s37, v252, 2
	v_mbcnt_lo_u32_b32 v34, -1, 0
	v_mbcnt_hi_u32_b32 v34, -1, v34
	v_readlane_b32 s2, v252, 6
	v_readlane_b32 s3, v252, 7
	s_add_i32 s46, s2, s3
	s_cmp_lt_u32 s2, 4
	s_cbranch_scc1 .Lp1_normal
	v_readlane_b32 s98, v255, 62
	s_cmp_lg_u32 s98, 0
	s_cbranch_scc1 .Lp1_normal
	s_mov_b32 s98, 1
	v_writelane_b32 v255, s98, 62
	s_branch .LBB0_44
.Lp1_normal:
	s_cmpk_gt_i32 s46, 0x16ef
	s_cbranch_scc1 .LBB0_44
	v_lshlrev_b32_e32 v2, 3, v34
	v_and_b32_e32 v160, 56, v2
	s_lshl_b32 s3, s2, 14
	v_ashrrev_i32_e32 v1, 3, v34
	v_lshlrev_b32_e32 v0, 2, v34
	s_movk_i32 s6, 0x84
	v_lshlrev_b32_e32 v2, 1, v160
	v_mov_b32_e32 v3, v161
	s_add_i32 s3, s3, 0
	v_and_b32_e32 v0, 28, v0
	v_mul_lo_u32 v38, v1, s6
	v_mul_u32_u24_e32 v4, 0x84, v160
	v_lshl_add_u64 v[30:31], s[36:37], 0, v[2:3]
	s_mov_b64 s[6:7], 0x1960000
	v_lshlrev_b32_e32 v5, 2, v1
	v_lshl_add_u32 v37, v0, 2, s3
	v_lshl_add_u64 v[2:3], v[30:31], 0, s[6:7]
	v_add3_u32 v36, s3, v4, v5
	s_mov_b64 s[6:7], 0x18e0000
	v_readlane_b32 s3, v253, 42
	v_lshl_add_u64 v[4:5], v[30:31], 0, s[6:7]
	s_mov_b64 s[6:7], 0x1880000
	s_add_i32 s2, s3, s2
	s_waitcnt vmcnt(3)
	v_lshl_add_u64 v[6:7], v[30:31], 0, s[6:7]
	s_mov_b64 s[6:7], 0x1680000
	s_lshl_b32 s2, s2, 1
	v_lshl_add_u64 v[8:9], v[30:31], 0, s[6:7]
	s_and_b32 s7, s2, 0x1c0
	s_waitcnt vmcnt(1)
	v_add_u32_e32 v14, s7, v1
	v_ashrrev_i32_e32 v15, 31, v14
	v_lshlrev_b64 v[14:15], 12, v[14:15]
	s_mov_b64 s[2:3], 0x8000
	v_lshl_add_u64 v[16:17], v[14:15], 0, s[2:3]
	s_mov_b64 s[2:3], 0x18000
	v_lshl_add_u64 v[10:11], s[36:37], 0, v[160:161]
	s_mov_b64 s[10:11], 0xa80000
	s_waitcnt vmcnt(0)
	v_lshl_add_u64 v[20:21], v[14:15], 0, s[2:3]
	s_mov_b64 s[2:3], 0x28000
	v_lshl_add_u64 v[10:11], v[10:11], 0, s[10:11]
	s_mov_b64 s[10:11], 0x400000
	v_lshl_add_u64 v[24:25], v[14:15], 0, s[2:3]
	s_lshl_b32 s2, s7, 1
	s_mov_b32 s3, s97
	s_mul_i32 s38, s72, 0x328000
	s_mov_b32 s39, s97
	v_lshl_add_u64 v[12:13], v[30:31], 0, s[10:11]
	v_lshl_add_u64 v[30:31], v[30:31], 0, s[2:3]
	s_mov_b64 s[2:3], 0x1280000
	s_lshl_b32 s96, s72, 17
	s_mul_i32 s22, s72, 0x30000
	s_mov_b32 s23, s97
	v_lshl_add_u64 v[30:31], v[30:31], 0, s[2:3]
	s_lshl_b32 s2, s46, 1
	v_add_u32_e32 v37, v37, v38
	s_lshl_b64 s[42:43], s[38:39], 2
	s_mov_b32 s38, 0x6dc9c883
	s_lshl_b32 s18, s72, 20
	s_mov_b32 s19, s97
	v_add_u32_e32 v32, 8, v1
	v_add_u32_e32 v33, 16, v1
	v_add_u32_e32 v35, 24, v1
	s_lshl_b32 s6, s72, 2
	v_lshl_add_u64 v[18:19], v[14:15], 0, s[8:9]
	v_lshl_add_u64 v[22:23], v[14:15], 0, s[14:15]
	v_lshl_add_u64 v[26:27], v[14:15], 0, s[16:17]
	v_lshl_add_u64 v[28:29], v[14:15], 0, s[20:21]
	s_lshl_b32 s7, s46, 5
	s_add_i32 s10, s2, 0xfffff360
	v_add_u32_e32 v38, 0x420, v37
	v_add_u32_e32 v39, 0x428, v37
	v_add_u32_e32 v40, 0x840, v37
	v_add_u32_e32 v41, 0x848, v37
	v_add_u32_e32 v42, 0xc60, v37
	v_add_u32_e32 v43, 0xc68, v37
	v_add_u32_e32 v44, 0x1080, v37
	v_add_u32_e32 v45, 0x1088, v37
	v_add_u32_e32 v46, 0x14a0, v37
	s_lshl_b64 s[34:35], s[96:97], 2
	s_lshl_b64 s[40:41], s[22:23], 2
	s_mov_b32 s39, 0x3fc45f30
	s_mov_b32 s11, s46
	s_branch .LBB0_20

.LBB0_50:
	s_or_b64 exec, exec, s[2:3]
	v_readlane_b32 s6, v255, 36
	v_readlane_b32 s7, v255, 37
	s_mov_b64 s[2:3], -1
	s_and_b64 vcc, exec, s[6:7]
	v_ashrrev_i32_e32 v35, 31, v34
	v_readlane_b32 s98, v255, 62
	s_cmp_eq_u32 s98, 2
	s_cbranch_scc0 .Lp1_c50
	s_mov_b32 s98, 0
	v_writelane_b32 v255, s98, 62
	s_branch .LBB0_68
.Lp1_c50:
	s_cbranch_vccz .LBB0_57
	v_readlane_b32 s2, v254, 29
	s_cmpk_gt_i32 s46, 0x7fff
	s_mov_b32 s10, 0x1b400000
	v_mov_b32_e32 v0, s2
	v_readlane_b32 s2, v254, 30
	ds_read_b32 v0, v0
	s_mov_b32 s11, 0x23400000
	v_mov_b32_e32 v1, s2
	ds_read_b32 v1, v1
	s_waitcnt lgkmcnt(1)
	v_readfirstlane_b32 s2, v0
	s_waitcnt lgkmcnt(0)
	v_readfirstlane_b32 s3, v1
	s_cbranch_scc1 .LBB0_56
	s_ashr_i32 s47, s46, 31
	v_lshl_add_u64 v[0:1], v[34:35], 4, s[2:3]
	s_lshl_b64 s[2:3], s[46:47], 11
	s_add_u32 s6, s36, s2
	s_addc_u32 s7, s37, s3
	s_waitcnt vmcnt(1)
	v_lshlrev_b64 v[16:17], 3, v[34:35]
	v_lshl_add_u64 v[2:3], s[6:7], 0, v[16:17]
	s_mov_b64 s[6:7], 0x2400000
	v_add_co_u32_e32 v8, vcc, 0x1000, v0
	v_lshl_add_u64 v[4:5], v[2:3], 0, s[6:7]
	s_mov_b32 s6, 0x2400000
	s_mov_b64 s[34:35], vcc
	v_add_co_u32_e32 v2, vcc, s6, v2
	s_mov_b64 s[6:7], 0x1000
	s_nop 0
	v_addc_co_u32_e32 v3, vcc, 0, v3, vcc
	v_lshl_add_u64 v[12:13], v[0:1], 0, s[6:7]
	v_addc_co_u32_e64 v9, vcc, 0, v1, s[34:35]
	global_load_dwordx2 v[18:19], v[4:5], off offset:512
	global_load_dwordx2 v[24:25], v[4:5], off offset:1024
	global_load_dwordx2 v[28:29], v[2:3], off
	global_load_dwordx2 v[30:31], v[4:5], off offset:1536
	s_nop 0
	global_load_dwordx4 v[0:3], v[12:13], off offset:1024
	global_load_dwordx4 v[4:7], v[12:13], off offset:2048
	s_nop 0
	global_load_dwordx4 v[8:11], v[8:9], off
	s_nop 0
	global_load_dwordx4 v[12:15], v[12:13], off offset:3072
	v_lshl_add_u64 v[36:37], s[2:3], 0, v[16:17]
	s_lshl_b64 s[2:3], s[46:47], 10
	s_mov_b32 s6, s46
	v_lshl_add_u64 v[38:39], v[34:35], 2, s[2:3]
	s_waitcnt vmcnt(7)
	v_lshlrev_b32_e32 v16, 16, v18
	v_and_b32_e32 v17, 0xffff0000, v18
	v_lshlrev_b32_e32 v20, 16, v19
	v_and_b32_e32 v19, 0xffff0000, v19
	s_waitcnt vmcnt(6)
	v_lshlrev_b32_e32 v22, 16, v24
	v_and_b32_e32 v23, 0xffff0000, v24
	v_lshlrev_b32_e32 v26, 16, v25
	v_and_b32_e32 v27, 0xffff0000, v25
	s_waitcnt vmcnt(5)
	v_lshlrev_b32_e32 v18, 16, v28
	v_and_b32_e32 v21, 0xffff0000, v28
	v_lshlrev_b32_e32 v24, 16, v29
	v_and_b32_e32 v25, 0xffff0000, v29
	s_waitcnt vmcnt(4)
	v_lshlrev_b32_e32 v28, 16, v30
	v_and_b32_e32 v29, 0xffff0000, v30
	v_lshlrev_b32_e32 v30, 16, v31
	v_and_b32_e32 v31, 0xffff0000, v31
	v_mov_b32_e32 v50, v16
	v_mov_b32_e32 v51, v17
	v_mov_b32_e32 v48, v20
	v_mov_b32_e32 v49, v19
	v_mov_b32_e32 v46, v22
	v_mov_b32_e32 v47, v23
	v_mov_b32_e32 v42, v26
	v_mov_b32_e32 v43, v27
	v_mov_b32_e32 v54, v18
	v_mov_b32_e32 v55, v21
	v_mov_b32_e32 v52, v24
	v_mov_b32_e32 v53, v25
	v_mov_b32_e32 v44, v28
	v_mov_b32_e32 v45, v29
	v_mov_b32_e32 v40, v30
	v_mov_b32_e32 v41, v31
	s_branch .LBB0_54

.LBB0_68:
	v_readlane_b32 s98, v255, 62
	s_cmp_eq_u32 s98, 1
	s_cbranch_scc0 .Lp1_c68
	s_mov_b32 s98, 2
	v_writelane_b32 v255, s98, 62
	s_branch .LBB0_17
